# K3 output stores transposed through LDS into full-line coalesced stores
# speedup vs baseline: 1.0295x; 1.0295x over previous
.LBB2_350:
	v_readfirstlane_b32 s91, v0
	v_and_b32_e32 v1, 0x3c0, v0
	s_lshr_b32 s91, s91, 6
	s_movk_i32 s0, 0x31f
	v_cmp_gt_u32_e32 vcc, s0, v1
	s_and_saveexec_b64 s[0:1], vcc
	s_cbranch_execz .LBB2_371
	s_andn2_b64 vcc, exec, s[4:5]
	s_cbranch_vccnz .LBB2_365
	v_add_u32_e32 v1, 8, v46
	v_mov_b32_e32 v43, 0x3f80
	v_mov_b32_e32 v42, 1.0
	v_cmp_le_u32_e32 vcc, v1, v47
	v_mov_b32_e32 v7, 0
	v_mov_b32_e32 v6, 0
	v_mov_b32_e32 v9, 0
	v_mov_b32_e32 v8, 0
	v_mov_b32_e32 v3, 0
	v_mov_b32_e32 v2, 0
	v_mov_b32_e32 v5, 0
	v_mov_b32_e32 v4, 0
	s_and_saveexec_b64 s[0:1], vcc
	s_cbranch_execz .LBB2_356
	v_mov_b32_e32 v1, v44
	v_lshlrev_b32_e32 v45, 2, v46
	v_mov_b32_e32 v5, 0
	s_mov_b64 s[2:3], 0
	v_mov_b32_e32 v4, 0
	v_mov_b32_e32 v3, 0
	v_mov_b32_e32 v2, 0
	v_mov_b32_e32 v9, 0
	v_mov_b32_e32 v8, 0
	v_mov_b32_e32 v7, 0
	v_mov_b32_e32 v6, 0

.LBB2_369:
	v_xor_b32_e32 v0, 1, v51
	v_add_u32_e32 v1, 64, v52
	v_cmp_lt_i32_e32 vcc, v0, v1
	s_waitcnt lgkmcnt(0)
	v_mul_f32_e32 v2, v53, v2
	v_cndmask_b32_e32 v0, v51, v0, vcc
	v_lshlrev_b32_e32 v65, 2, v0
	v_mul_f32_e32 v0, v53, v6
	s_nop 1
	v_mov_b32_dpp v1, v0 quad_perm:[1,0,3,2] row_mask:0xf bank_mask:0xf
	v_cmp_eq_u32_e32 vcc, 0, v44
	v_mul_f32_e32 v6, v53, v7
	s_nop 1
	v_mov_b32_dpp v7, v6 quad_perm:[1,0,3,2] row_mask:0xf bank_mask:0xf
	s_waitcnt lgkmcnt(1)
	v_cndmask_b32_e32 v52, v1, v0, vcc
	v_cndmask_b32_e32 v70, v0, v1, vcc
	v_mul_f32_e32 v0, v53, v8
	s_nop 1
	v_mov_b32_dpp v1, v0 quad_perm:[1,0,3,2] row_mask:0xf bank_mask:0xf
	s_nop 1
	v_mov_b32_dpp v8, v2 quad_perm:[1,0,3,2] row_mask:0xf bank_mask:0xf
	s_waitcnt lgkmcnt(2)
	v_cndmask_b32_e32 v54, v7, v6, vcc
	v_cndmask_b32_e32 v68, v6, v7, vcc
	v_mul_f32_e32 v6, v53, v9
	s_waitcnt lgkmcnt(1)
	v_cndmask_b32_e32 v56, v1, v0, vcc
	v_cndmask_b32_e32 v76, v0, v1, vcc
	v_mul_f32_e32 v0, v53, v3
	s_nop 1
	v_mov_b32_dpp v1, v0 quad_perm:[1,0,3,2] row_mask:0xf bank_mask:0xf
	s_waitcnt lgkmcnt(1)
	v_cndmask_b32_e32 v60, v8, v2, vcc
	v_cndmask_b32_e32 v72, v2, v8, vcc
	v_mul_f32_e32 v2, v53, v4
	v_mul_f32_e32 v4, v53, v5
	s_nop 1
	v_mov_b32_dpp v5, v4 quad_perm:[1,0,3,2] row_mask:0xf bank_mask:0xf
	s_nop 1
	v_mov_b32_dpp v3, v2 quad_perm:[1,0,3,2] row_mask:0xf bank_mask:0xf
	s_nop 1
	v_mov_b32_dpp v7, v6 quad_perm:[1,0,3,2] row_mask:0xf bank_mask:0xf
	s_waitcnt lgkmcnt(3)
	v_cndmask_b32_e32 v62, v1, v0, vcc
	v_cndmask_b32_e32 v82, v0, v1, vcc
	v_mul_u32_u24_e32 v0, 20, v44
	v_lshlrev_b32_e32 v66, 2, v0
	s_waitcnt lgkmcnt(2)
	v_cndmask_b32_e32 v84, v5, v4, vcc
	v_cndmask_b32_e32 v78, v4, v5, vcc
	v_add_u32_e32 v66, 0x16400, v66
	s_waitcnt lgkmcnt(1)
	v_cndmask_b32_e32 v86, v3, v2, vcc
	v_cndmask_b32_e32 v80, v2, v3, vcc
	ds_read_b128 v[48:51], v66 offset:6224
	ds_read_b128 v[88:91], v66 offset:6240
	ds_read_b128 v[32:35], v66 offset:6256
	ds_read_b128 v[16:19], v66 offset:6272
	ds_read_b128 v[0:3], v66 offset:6288
	ds_read_b128 v[92:95], v66
	ds_read_b128 v[96:99], v66 offset:16
	ds_read_b128 v[40:43], v66 offset:32
	s_waitcnt lgkmcnt(8)
	v_cndmask_b32_e32 v58, v7, v6, vcc
	v_cndmask_b32_e32 v74, v6, v7, vcc
	ds_read_b128 v[20:23], v66 offset:48
	ds_read_b128 v[4:7], v66 offset:64
	ds_read_b128 v[100:103], v66 offset:160
	ds_read_b128 v[104:107], v66 offset:176
	ds_read_b128 v[36:39], v66 offset:192
	ds_read_b128 v[24:27], v66 offset:208
	s_waitcnt vmcnt(0)
	ds_read_b128 v[8:11], v66 offset:224
	ds_read_b128 v[108:111], v66 offset:320
	ds_read_b128 v[112:115], v66 offset:336
	ds_read_b128 v[44:47], v66 offset:352
	ds_read_b128 v[28:31], v66 offset:368
	ds_read_b128 v[12:15], v66 offset:384
	s_waitcnt lgkmcnt(14)
	v_pk_fma_f32 v[48:49], v[52:53], v[92:93], v[48:49] op_sel_hi:[0,1,1]
	v_pk_fma_f32 v[50:51], v[52:53], v[94:95], v[50:51] op_sel_hi:[0,1,1]
	ds_read_b128 v[92:95], v66 offset:480
	ds_read_b128 v[116:119], v66 offset:496
	s_waitcnt lgkmcnt(11)
	v_pk_fma_f32 v[48:49], v[54:55], v[100:101], v[48:49] op_sel_hi:[0,1,1]
	v_pk_fma_f32 v[50:51], v[54:55], v[102:103], v[50:51] op_sel_hi:[0,1,1]
	ds_read_b128 v[120:123], v66 offset:512
	ds_read_b128 v[124:127], v66 offset:528
	s_waitcnt lgkmcnt(8)
	v_pk_fma_f32 v[100:101], v[56:57], v[108:109], v[48:49] op_sel_hi:[0,1,1]
	v_pk_fma_f32 v[102:103], v[56:57], v[110:111], v[50:51] op_sel_hi:[0,1,1]
	v_pk_fma_f32 v[96:97], v[52:53], v[96:97], v[88:89] op_sel_hi:[0,1,1]
	v_pk_fma_f32 v[108:109], v[52:53], v[98:99], v[90:91] op_sel_hi:[0,1,1]
	ds_read_b128 v[48:51], v66 offset:544
	ds_read_b128 v[88:91], v66 offset:640
	s_waitcnt lgkmcnt(5)
	v_pk_fma_f32 v[98:99], v[58:59], v[92:93], v[100:101] op_sel_hi:[0,1,1]
	v_pk_fma_f32 v[100:101], v[58:59], v[94:95], v[102:103] op_sel_hi:[0,1,1]
	ds_read_b128 v[92:95], v66 offset:800
	s_waitcnt lgkmcnt(1)
	v_pk_fma_f32 v[98:99], v[60:61], v[88:89], v[98:99] op_sel_hi:[0,1,1]
	v_pk_fma_f32 v[100:101], v[60:61], v[90:91], v[100:101] op_sel_hi:[0,1,1]
	ds_read_b128 v[88:91], v66 offset:816
	s_waitcnt lgkmcnt(1)
	v_pk_fma_f32 v[98:99], v[62:63], v[92:93], v[98:99] op_sel_hi:[0,1,1]
	v_pk_fma_f32 v[92:93], v[62:63], v[94:95], v[100:101] op_sel_hi:[0,1,1]
	v_pk_fma_f32 v[100:101], v[54:55], v[104:105], v[96:97] op_sel_hi:[0,1,1]
	v_pk_fma_f32 v[102:103], v[54:55], v[106:107], v[108:109] op_sel_hi:[0,1,1]
	ds_read_b128 v[94:97], v66 offset:656
	ds_read_b128 v[108:111], v66 offset:672
	v_pk_fma_f32 v[100:101], v[56:57], v[112:113], v[100:101] op_sel_hi:[0,1,1]
	v_pk_fma_f32 v[102:103], v[56:57], v[114:115], v[102:103] op_sel_hi:[0,1,1]
	v_pk_fma_f32 v[100:101], v[58:59], v[116:117], v[100:101] op_sel_hi:[0,1,1]
	v_pk_fma_f32 v[102:103], v[58:59], v[118:119], v[102:103] op_sel_hi:[0,1,1]
	ds_read_b128 v[112:115], v66 offset:688
	ds_read_b128 v[116:119], v66 offset:704
	v_pk_fma_f32 v[32:33], v[52:53], v[40:41], v[32:33] op_sel_hi:[0,1,1]
	v_pk_fma_f32 v[32:33], v[54:55], v[36:37], v[32:33] op_sel_hi:[0,1,1]
	v_pk_fma_f32 v[32:33], v[56:57], v[44:45], v[32:33] op_sel_hi:[0,1,1]
	s_waitcnt lgkmcnt(3)
	v_pk_fma_f32 v[94:95], v[60:61], v[94:95], v[100:101] op_sel_hi:[0,1,1]
	v_pk_fma_f32 v[32:33], v[58:59], v[120:121], v[32:33] op_sel_hi:[0,1,1]
	v_pk_fma_f32 v[106:107], v[62:63], v[88:89], v[94:95] op_sel_hi:[0,1,1]
	v_pk_fma_f32 v[88:89], v[60:61], v[96:97], v[102:103] op_sel_hi:[0,1,1]
	s_waitcnt lgkmcnt(2)
	v_pk_fma_f32 v[36:37], v[60:61], v[108:109], v[32:33] op_sel_hi:[0,1,1]
	v_pk_fma_f32 v[104:105], v[62:63], v[90:91], v[88:89] op_sel_hi:[0,1,1]
	ds_read_b128 v[88:91], v66 offset:832
	v_pk_fma_f32 v[40:41], v[52:53], v[42:43], v[34:35] op_sel_hi:[0,1,1]
	ds_read_b128 v[32:35], v66 offset:848
	v_pk_fma_f32 v[16:17], v[52:53], v[20:21], v[16:17] op_sel_hi:[0,1,1]
	v_pk_fma_f32 v[16:17], v[54:55], v[24:25], v[16:17] op_sel_hi:[0,1,1]
	v_pk_fma_f32 v[16:17], v[56:57], v[28:29], v[16:17] op_sel_hi:[0,1,1]
	v_pk_fma_f32 v[16:17], v[58:59], v[124:125], v[16:17] op_sel_hi:[0,1,1]
	s_waitcnt lgkmcnt(3)
	v_pk_fma_f32 v[16:17], v[60:61], v[112:113], v[16:17] op_sel_hi:[0,1,1]
	s_waitcnt lgkmcnt(1)
	v_pk_fma_f32 v[102:103], v[62:63], v[88:89], v[36:37] op_sel_hi:[0,1,1]
	s_waitcnt lgkmcnt(0)
	v_pk_fma_f32 v[88:89], v[62:63], v[32:33], v[16:17] op_sel_hi:[0,1,1]
	v_pk_fma_f32 v[16:17], v[52:53], v[22:23], v[18:19] op_sel_hi:[0,1,1]
	v_pk_fma_f32 v[16:17], v[54:55], v[26:27], v[16:17] op_sel_hi:[0,1,1]
	v_pk_fma_f32 v[16:17], v[56:57], v[30:31], v[16:17] op_sel_hi:[0,1,1]
	v_pk_fma_f32 v[16:17], v[58:59], v[126:127], v[16:17] op_sel_hi:[0,1,1]
	v_pk_fma_f32 v[16:17], v[60:61], v[114:115], v[16:17] op_sel_hi:[0,1,1]
	v_pk_fma_f32 v[94:95], v[62:63], v[34:35], v[16:17] op_sel_hi:[0,1,1]
	ds_read_b128 v[16:19], v66 offset:864
	v_pk_fma_f32 v[0:1], v[52:53], v[4:5], v[0:1] op_sel_hi:[0,1,1]
	v_pk_fma_f32 v[0:1], v[54:55], v[8:9], v[0:1] op_sel_hi:[0,1,1]
	v_pk_fma_f32 v[0:1], v[56:57], v[12:13], v[0:1] op_sel_hi:[0,1,1]
	v_pk_fma_f32 v[0:1], v[58:59], v[48:49], v[0:1] op_sel_hi:[0,1,1]
	v_pk_fma_f32 v[0:1], v[60:61], v[116:117], v[0:1] op_sel_hi:[0,1,1]
	ds_read_b128 v[32:35], v66 offset:960
	s_waitcnt lgkmcnt(1)
	v_pk_fma_f32 v[96:97], v[62:63], v[16:17], v[0:1] op_sel_hi:[0,1,1]
	v_pk_fma_f32 v[0:1], v[52:53], v[6:7], v[2:3] op_sel_hi:[0,1,1]
	v_pk_fma_f32 v[36:37], v[54:55], v[38:39], v[40:41] op_sel_hi:[0,1,1]
	v_pk_fma_f32 v[0:1], v[54:55], v[10:11], v[0:1] op_sel_hi:[0,1,1]
	v_pk_fma_f32 v[36:37], v[56:57], v[46:47], v[36:37] op_sel_hi:[0,1,1]
	v_pk_fma_f32 v[0:1], v[56:57], v[14:15], v[0:1] op_sel_hi:[0,1,1]
	v_pk_fma_f32 v[36:37], v[58:59], v[122:123], v[36:37] op_sel_hi:[0,1,1]
	v_pk_fma_f32 v[0:1], v[58:59], v[50:51], v[0:1] op_sel_hi:[0,1,1]
	v_pk_fma_f32 v[36:37], v[60:61], v[110:111], v[36:37] op_sel_hi:[0,1,1]
	v_pk_fma_f32 v[0:1], v[60:61], v[118:119], v[0:1] op_sel_hi:[0,1,1]
	v_pk_fma_f32 v[100:101], v[62:63], v[90:91], v[36:37] op_sel_hi:[0,1,1]
	v_pk_fma_f32 v[90:91], v[62:63], v[18:19], v[0:1] op_sel_hi:[0,1,1]
	ds_read_b128 v[48:51], v66 offset:976
	ds_read_b128 v[28:31], v66 offset:992
	ds_read_b128 v[16:19], v66 offset:1008
	ds_read_b128 v[0:3], v66 offset:1024
	ds_read_b128 v[44:47], v66 offset:1120
	ds_read_b128 v[52:55], v66 offset:1136
	ds_read_b128 v[36:39], v66 offset:1152
	ds_read_b128 v[20:23], v66 offset:1168
	ds_read_b128 v[4:7], v66 offset:1184
	ds_read_b128 v[108:111], v66 offset:1280
	ds_read_b128 v[56:59], v66 offset:1296
	ds_read_b128 v[40:43], v66 offset:1312
	ds_read_b128 v[24:27], v66 offset:1328
	ds_read_b128 v[8:11], v66 offset:1344
	ds_read_b128 v[112:115], v66 offset:1440
	ds_read_b128 v[60:63], v66 offset:1456
	ds_read_b128 v[12:15], v66 offset:1504
	ds_read_b128 v[116:119], v66 offset:1600
	s_waitcnt lgkmcnt(14)
	v_pk_fma_f32 v[32:33], v[86:87], v[32:33], v[98:99] op_sel_hi:[0,1,1]
	v_pk_fma_f32 v[34:35], v[86:87], v[34:35], v[92:93] op_sel_hi:[0,1,1]
	s_waitcnt lgkmcnt(13)
	v_pk_fma_f32 v[32:33], v[84:85], v[44:45], v[32:33] op_sel_hi:[0,1,1]
	v_pk_fma_f32 v[34:35], v[84:85], v[46:47], v[34:35] op_sel_hi:[0,1,1]
	ds_read_b128 v[120:123], v66 offset:1760
	ds_read_b128 v[124:127], v66 offset:1776
	s_waitcnt lgkmcnt(10)
	v_pk_fma_f32 v[92:93], v[70:71], v[108:109], v[32:33] op_sel_hi:[0,1,1]
	v_pk_fma_f32 v[98:99], v[70:71], v[110:111], v[34:35] op_sel_hi:[0,1,1]
	ds_read_b128 v[32:35], v66 offset:1824
	ds_read_b128 v[44:47], v66 offset:1920
	s_waitcnt lgkmcnt(7)
	v_pk_fma_f32 v[92:93], v[68:69], v[112:113], v[92:93] op_sel_hi:[0,1,1]
	v_pk_fma_f32 v[98:99], v[68:69], v[114:115], v[98:99] op_sel_hi:[0,1,1]
	ds_read_b128 v[108:111], v66 offset:2080
	ds_read_b128 v[112:115], v66 offset:2096
	s_waitcnt lgkmcnt(6)
	v_pk_fma_f32 v[92:93], v[76:77], v[116:117], v[92:93] op_sel_hi:[0,1,1]
	v_pk_fma_f32 v[98:99], v[76:77], v[118:119], v[98:99] op_sel_hi:[0,1,1]
	s_waitcnt lgkmcnt(5)
	v_pk_fma_f32 v[92:93], v[74:75], v[120:121], v[92:93] op_sel_hi:[0,1,1]
	v_pk_fma_f32 v[98:99], v[74:75], v[122:123], v[98:99] op_sel_hi:[0,1,1]
	s_waitcnt lgkmcnt(2)
	v_pk_fma_f32 v[92:93], v[72:73], v[44:45], v[92:93] op_sel_hi:[0,1,1]
	v_pk_fma_f32 v[98:99], v[72:73], v[46:47], v[98:99] op_sel_hi:[0,1,1]
	ds_read_b128 v[44:47], v66 offset:2144
	ds_read_b128 v[116:119], v66 offset:2240
	s_waitcnt lgkmcnt(3)
	v_pk_fma_f32 v[92:93], v[82:83], v[108:109], v[92:93] op_sel_hi:[0,1,1]
	v_pk_fma_f32 v[98:99], v[82:83], v[110:111], v[98:99] op_sel_hi:[0,1,1]
	ds_read_b128 v[108:111], v66 offset:2400
	s_waitcnt lgkmcnt(1)
	v_pk_fma_f32 v[92:93], v[80:81], v[116:117], v[92:93] op_sel_hi:[0,1,1]
	v_pk_fma_f32 v[98:99], v[80:81], v[118:119], v[98:99] op_sel_hi:[0,1,1]
	s_waitcnt lgkmcnt(0)
	v_pk_fma_f32 v[92:93], v[78:79], v[108:109], v[92:93] op_sel_hi:[0,1,1]
	v_pk_fma_f32 v[98:99], v[78:79], v[110:111], v[98:99] op_sel_hi:[0,1,1]
	v_pk_fma_f32 v[108:109], v[86:87], v[48:49], v[106:107] op_sel_hi:[0,1,1]
	v_pk_fma_f32 v[110:111], v[86:87], v[50:51], v[104:105] op_sel_hi:[0,1,1]
	ds_read_b128 v[116:119], v66 offset:2416
	ds_read_b128 v[104:107], v66 offset:1472
	ds_read_b128 v[48:51], v66 offset:1488
	v_pk_fma_f32 v[52:53], v[84:85], v[52:53], v[108:109] op_sel_hi:[0,1,1]
	v_pk_fma_f32 v[54:55], v[84:85], v[54:55], v[110:111] op_sel_hi:[0,1,1]
	v_pk_fma_f32 v[56:57], v[70:71], v[56:57], v[52:53] op_sel_hi:[0,1,1]
	v_pk_fma_f32 v[58:59], v[70:71], v[58:59], v[54:55] op_sel_hi:[0,1,1]
	ds_read_b128 v[52:55], v66 offset:1616
	ds_read_b128 v[108:111], v66 offset:1632
	v_pk_fma_f32 v[56:57], v[68:69], v[60:61], v[56:57] op_sel_hi:[0,1,1]
	v_pk_fma_f32 v[58:59], v[68:69], v[62:63], v[58:59] op_sel_hi:[0,1,1]
	s_waitcnt lgkmcnt(1)
	v_pk_fma_f32 v[56:57], v[76:77], v[52:53], v[56:57] op_sel_hi:[0,1,1]
	v_pk_fma_f32 v[58:59], v[76:77], v[54:55], v[58:59] op_sel_hi:[0,1,1]
	ds_read_b128 v[52:55], v66 offset:1936
	v_pk_fma_f32 v[56:57], v[74:75], v[124:125], v[56:57] op_sel_hi:[0,1,1]
	v_pk_fma_f32 v[58:59], v[74:75], v[126:127], v[58:59] op_sel_hi:[0,1,1]
	ds_read_b128 v[60:63], v66 offset:1952
	s_waitcnt lgkmcnt(1)
	v_pk_fma_f32 v[56:57], v[72:73], v[52:53], v[56:57] op_sel_hi:[0,1,1]
	v_pk_fma_f32 v[58:59], v[72:73], v[54:55], v[58:59] op_sel_hi:[0,1,1]
	ds_read_b128 v[52:55], v66 offset:2256
	v_pk_fma_f32 v[56:57], v[82:83], v[112:113], v[56:57] op_sel_hi:[0,1,1]
	v_pk_fma_f32 v[58:59], v[82:83], v[114:115], v[58:59] op_sel_hi:[0,1,1]
	s_waitcnt lgkmcnt(0)
	v_pk_fma_f32 v[56:57], v[80:81], v[52:53], v[56:57] op_sel_hi:[0,1,1]
	v_pk_fma_f32 v[58:59], v[80:81], v[54:55], v[58:59] op_sel_hi:[0,1,1]
	v_pk_fma_f32 v[56:57], v[78:79], v[116:117], v[56:57] op_sel_hi:[0,1,1]
	v_pk_fma_f32 v[58:59], v[78:79], v[118:119], v[58:59] op_sel_hi:[0,1,1]
	v_pk_fma_f32 v[116:117], v[86:87], v[28:29], v[102:103] op_sel_hi:[0,1,1]
	v_pk_fma_f32 v[118:119], v[86:87], v[30:31], v[100:101] op_sel_hi:[0,1,1]
	ds_read_b128 v[112:115], v66 offset:2272
	ds_read_b128 v[120:123], v66 offset:1648
	ds_read_b128 v[52:55], v66 offset:1664
	v_pk_fma_f32 v[36:37], v[84:85], v[36:37], v[116:117] op_sel_hi:[0,1,1]
	v_pk_fma_f32 v[38:39], v[84:85], v[38:39], v[118:119] op_sel_hi:[0,1,1]
	ds_read_b128 v[28:31], v66 offset:1792
	ds_read_b128 v[100:103], v66 offset:1808
	v_pk_fma_f32 v[116:117], v[70:71], v[40:41], v[36:37] op_sel_hi:[0,1,1]
	v_pk_fma_f32 v[118:119], v[70:71], v[42:43], v[38:39] op_sel_hi:[0,1,1]
	ds_read_b128 v[36:39], v66 offset:1968
	ds_read_b128 v[40:43], v66 offset:1984
	v_pk_fma_f32 v[104:105], v[68:69], v[104:105], v[116:117] op_sel_hi:[0,1,1]
	v_pk_fma_f32 v[106:107], v[68:69], v[106:107], v[118:119] op_sel_hi:[0,1,1]
	v_pk_fma_f32 v[116:117], v[76:77], v[108:109], v[104:105] op_sel_hi:[0,1,1]
	v_pk_fma_f32 v[118:119], v[76:77], v[110:111], v[106:107] op_sel_hi:[0,1,1]
	ds_read_b128 v[104:107], v66 offset:2112
	ds_read_b128 v[108:111], v66 offset:2128
	s_waitcnt lgkmcnt(5)
	v_pk_fma_f32 v[28:29], v[74:75], v[28:29], v[116:117] op_sel_hi:[0,1,1]
	v_pk_fma_f32 v[30:31], v[74:75], v[30:31], v[118:119] op_sel_hi:[0,1,1]
	v_pk_fma_f32 v[16:17], v[86:87], v[16:17], v[88:89] op_sel_hi:[0,1,1]
	v_pk_fma_f32 v[28:29], v[72:73], v[60:61], v[28:29] op_sel_hi:[0,1,1]
	v_pk_fma_f32 v[30:31], v[72:73], v[62:63], v[30:31] op_sel_hi:[0,1,1]
	ds_read_b128 v[60:63], v66 offset:2288
	ds_read_b128 v[116:119], v66 offset:2304
	v_pk_fma_f32 v[16:17], v[84:85], v[20:21], v[16:17] op_sel_hi:[0,1,1]
	v_pk_fma_f32 v[18:19], v[86:87], v[18:19], v[94:95] op_sel_hi:[0,1,1]
	s_waitcnt lgkmcnt(3)
	v_pk_fma_f32 v[104:105], v[82:83], v[104:105], v[28:29] op_sel_hi:[0,1,1]
	v_pk_fma_f32 v[106:107], v[82:83], v[106:107], v[30:31] op_sel_hi:[0,1,1]
	ds_read_b128 v[28:31], v66 offset:2432
	v_pk_fma_f32 v[16:17], v[70:71], v[24:25], v[16:17] op_sel_hi:[0,1,1]
	v_pk_fma_f32 v[18:19], v[84:85], v[22:23], v[18:19] op_sel_hi:[0,1,1]
	v_pk_fma_f32 v[0:1], v[86:87], v[0:1], v[96:97] op_sel_hi:[0,1,1]
	v_pk_fma_f32 v[16:17], v[68:69], v[48:49], v[16:17] op_sel_hi:[0,1,1]
	v_pk_fma_f32 v[18:19], v[70:71], v[26:27], v[18:19] op_sel_hi:[0,1,1]
	ds_read_b128 v[20:23], v66 offset:2464
	v_pk_fma_f32 v[0:1], v[84:85], v[4:5], v[0:1] op_sel_hi:[0,1,1]
	v_pk_fma_f32 v[2:3], v[86:87], v[2:3], v[90:91] op_sel_hi:[0,1,1]
	v_pk_fma_f32 v[112:113], v[80:81], v[112:113], v[104:105] op_sel_hi:[0,1,1]
	v_pk_fma_f32 v[114:115], v[80:81], v[114:115], v[106:107] op_sel_hi:[0,1,1]
	ds_read_b128 v[104:107], v66 offset:2448
	v_subrev_u32_e32 v66, 0x16400, v66
	v_pk_fma_f32 v[16:17], v[76:77], v[120:121], v[16:17] op_sel_hi:[0,1,1]
	v_pk_fma_f32 v[18:19], v[68:69], v[50:51], v[18:19] op_sel_hi:[0,1,1]
	v_pk_fma_f32 v[0:1], v[70:71], v[8:9], v[0:1] op_sel_hi:[0,1,1]
	v_pk_fma_f32 v[2:3], v[84:85], v[6:7], v[2:3] op_sel_hi:[0,1,1]
	v_max_f32_e32 v4, v92, v93
	v_pk_fma_f32 v[16:17], v[74:75], v[100:101], v[16:17] op_sel_hi:[0,1,1]
	v_pk_fma_f32 v[18:19], v[76:77], v[122:123], v[18:19] op_sel_hi:[0,1,1]
	v_pk_fma_f32 v[0:1], v[68:69], v[12:13], v[0:1] op_sel_hi:[0,1,1]
	v_pk_fma_f32 v[2:3], v[70:71], v[10:11], v[2:3] op_sel_hi:[0,1,1]
	v_max3_f32 v4, v4, v98, v99
	v_pk_fma_f32 v[16:17], v[72:73], v[36:37], v[16:17] op_sel_hi:[0,1,1]
	v_pk_fma_f32 v[18:19], v[74:75], v[102:103], v[18:19] op_sel_hi:[0,1,1]
	v_pk_fma_f32 v[0:1], v[76:77], v[52:53], v[0:1] op_sel_hi:[0,1,1]
	v_pk_fma_f32 v[2:3], v[68:69], v[14:15], v[2:3] op_sel_hi:[0,1,1]
	v_max3_f32 v4, v4, v56, v57
	s_waitcnt lgkmcnt(2)
	v_pk_fma_f32 v[28:29], v[78:79], v[28:29], v[112:113] op_sel_hi:[0,1,1]
	v_pk_fma_f32 v[16:17], v[82:83], v[108:109], v[16:17] op_sel_hi:[0,1,1]
	v_pk_fma_f32 v[18:19], v[72:73], v[38:39], v[18:19] op_sel_hi:[0,1,1]
	v_pk_fma_f32 v[0:1], v[74:75], v[32:33], v[0:1] op_sel_hi:[0,1,1]
	v_pk_fma_f32 v[2:3], v[76:77], v[54:55], v[2:3] op_sel_hi:[0,1,1]
	v_max3_f32 v4, v4, v58, v59
	v_pk_fma_f32 v[30:31], v[78:79], v[30:31], v[114:115] op_sel_hi:[0,1,1]
	v_pk_fma_f32 v[16:17], v[80:81], v[60:61], v[16:17] op_sel_hi:[0,1,1]
	v_pk_fma_f32 v[18:19], v[82:83], v[110:111], v[18:19] op_sel_hi:[0,1,1]
	v_pk_fma_f32 v[0:1], v[72:73], v[40:41], v[0:1] op_sel_hi:[0,1,1]
	v_pk_fma_f32 v[2:3], v[74:75], v[34:35], v[2:3] op_sel_hi:[0,1,1]
	v_max3_f32 v4, v4, v28, v29
	s_waitcnt lgkmcnt(0)
	v_pk_fma_f32 v[16:17], v[78:79], v[104:105], v[16:17] op_sel_hi:[0,1,1]
	v_pk_fma_f32 v[18:19], v[80:81], v[62:63], v[18:19] op_sel_hi:[0,1,1]
	v_pk_fma_f32 v[0:1], v[82:83], v[44:45], v[0:1] op_sel_hi:[0,1,1]
	v_pk_fma_f32 v[2:3], v[72:73], v[42:43], v[2:3] op_sel_hi:[0,1,1]
	v_max3_f32 v4, v4, v30, v31
	v_pk_fma_f32 v[18:19], v[78:79], v[106:107], v[18:19] op_sel_hi:[0,1,1]
	v_pk_fma_f32 v[0:1], v[80:81], v[116:117], v[0:1] op_sel_hi:[0,1,1]
	v_pk_fma_f32 v[2:3], v[82:83], v[46:47], v[2:3] op_sel_hi:[0,1,1]
	v_max3_f32 v4, v4, v16, v17
	v_pk_fma_f32 v[0:1], v[78:79], v[20:21], v[0:1] op_sel_hi:[0,1,1]
	v_pk_fma_f32 v[2:3], v[80:81], v[118:119], v[2:3] op_sel_hi:[0,1,1]
	v_max3_f32 v4, v4, v18, v19
	v_pk_fma_f32 v[2:3], v[78:79], v[22:23], v[2:3] op_sel_hi:[0,1,1]
	v_max3_f32 v4, v4, v0, v1
	v_max3_f32 v4, v4, v2, v3
	s_nop 1
	v_mov_b32_dpp v5, v4 quad_perm:[1,0,3,2] row_mask:0xf bank_mask:0xf
	s_waitcnt lgkmcnt(0)
	v_max_f32_e32 v5, v5, v5
	v_max_f32_e32 v4, v4, v5
	v_sub_f32_e32 v5, v92, v4
	v_mul_f32_e32 v5, 0x3fb8aa3b, v5
	v_sub_f32_e32 v6, v93, v4
	v_exp_f32_e32 v5, v5
	v_mul_f32_e32 v6, 0x3fb8aa3b, v6
	v_sub_f32_e32 v7, v98, v4
	v_exp_f32_e32 v6, v6
	v_mul_f32_e32 v7, 0x3fb8aa3b, v7
	v_sub_f32_e32 v8, v99, v4
	v_exp_f32_e32 v7, v7
	v_mul_f32_e32 v8, 0x3fb8aa3b, v8
	v_exp_f32_e32 v8, v8
	v_add_f32_e32 v5, 0, v5
	v_add_f32_e32 v5, v5, v6
	v_sub_f32_e32 v6, v56, v4
	v_add_f32_e32 v5, v5, v7
	v_mul_f32_e32 v6, 0x3fb8aa3b, v6
	v_sub_f32_e32 v7, v57, v4
	v_add_f32_e32 v5, v5, v8
	v_exp_f32_e32 v6, v6
	v_mul_f32_e32 v7, 0x3fb8aa3b, v7
	v_sub_f32_e32 v8, v58, v4
	v_exp_f32_e32 v7, v7
	v_mul_f32_e32 v8, 0x3fb8aa3b, v8
	v_sub_f32_e32 v9, v59, v4
	v_exp_f32_e32 v8, v8
	v_mul_f32_e32 v9, 0x3fb8aa3b, v9
	v_exp_f32_e32 v9, v9
	v_add_f32_e32 v5, v5, v6
	v_sub_f32_e32 v6, v28, v4
	v_add_f32_e32 v5, v5, v7
	v_mul_f32_e32 v6, 0x3fb8aa3b, v6
	v_sub_f32_e32 v7, v29, v4
	v_add_f32_e32 v5, v5, v8
	v_exp_f32_e32 v6, v6
	v_mul_f32_e32 v7, 0x3fb8aa3b, v7
	v_sub_f32_e32 v8, v30, v4
	v_add_f32_e32 v5, v5, v9
	v_exp_f32_e32 v7, v7
	v_mul_f32_e32 v8, 0x3fb8aa3b, v8
	v_sub_f32_e32 v9, v31, v4
	v_exp_f32_e32 v8, v8
	v_mul_f32_e32 v9, 0x3fb8aa3b, v9
	v_exp_f32_e32 v9, v9
	v_add_f32_e32 v5, v5, v6
	v_sub_f32_e32 v6, v16, v4
	v_add_f32_e32 v5, v5, v7
	v_mul_f32_e32 v6, 0x3fb8aa3b, v6
	v_sub_f32_e32 v7, v17, v4
	v_add_f32_e32 v5, v5, v8
	v_exp_f32_e32 v6, v6
	v_mul_f32_e32 v7, 0x3fb8aa3b, v7
	v_sub_f32_e32 v8, v18, v4
	v_add_f32_e32 v5, v5, v9
	v_exp_f32_e32 v7, v7
	v_mul_f32_e32 v8, 0x3fb8aa3b, v8
	v_sub_f32_e32 v9, v19, v4
	v_exp_f32_e32 v8, v8
	v_mul_f32_e32 v9, 0x3fb8aa3b, v9
	v_exp_f32_e32 v9, v9
	v_add_f32_e32 v5, v5, v6
	v_sub_f32_e32 v6, v0, v4
	v_add_f32_e32 v5, v5, v7
	v_mul_f32_e32 v6, 0x3fb8aa3b, v6
	v_sub_f32_e32 v7, v1, v4
	v_add_f32_e32 v5, v5, v8
	v_exp_f32_e32 v6, v6
	v_mul_f32_e32 v7, 0x3fb8aa3b, v7
	v_sub_f32_e32 v8, v2, v4
	v_add_f32_e32 v5, v5, v9
	v_exp_f32_e32 v7, v7
	v_mul_f32_e32 v8, 0x3fb8aa3b, v8
	v_sub_f32_e32 v9, v3, v4
	v_exp_f32_e32 v8, v8
	v_mul_f32_e32 v9, 0x3fb8aa3b, v9
	v_exp_f32_e32 v9, v9
	v_add_f32_e32 v5, v5, v6
	v_add_f32_e32 v5, v5, v7
	v_add_f32_e32 v5, v5, v8
	v_add_f32_e32 v5, v5, v9
	s_nop 1
	v_mov_b32_dpp v6, v5 quad_perm:[1,0,3,2] row_mask:0xf bank_mask:0xf
	s_and_b64 exec, exec, s[8:9]
	s_cbranch_execz .LBB2_371
	s_waitcnt lgkmcnt(0)
	v_add_f32_e32 v5, v5, v6
	s_mov_b32 s0, 0x800000
	v_cmp_gt_f32_e32 vcc, s0, v5
	s_mov_b32 s0, 0x3f317217
	v_mov_b32_e32 v67, 0
	v_cndmask_b32_e64 v6, 0, 32, vcc
	v_ldexp_f32 v5, v5, v6
	v_log_f32_e32 v5, v5
	s_nop 0
	v_mul_f32_e32 v6, 0x3f317217, v5
	v_fma_f32 v6, v5, s0, -v6
	v_fmamk_f32 v6, v5, 0x3377d1cf, v6
	s_mov_b32 s0, 0x7f800000
	v_fmac_f32_e32 v6, 0x3f317217, v5
	v_cmp_lt_f32_e64 s[0:1], |v5|, s0
	s_nop 1
	v_cndmask_b32_e64 v5, v5, v6, s[0:1]
	v_mov_b32_e32 v6, 0x41b17218
	v_cndmask_b32_e32 v6, 0, v6, vcc
	v_sub_f32_e32 v5, v5, v6
	v_add_f32_e32 v10, v4, v5
	s_mov_b64 s[0:1], exec
	s_bcnt1_i32_b64 s94, exec
	s_mulk_i32 s94, 0x50
	s_lshl_b32 s92, s91, 5
	s_add_i32 s92, s92, s64
	s_mulk_i32 s92, 0xa0
	s_add_u32 s92, s52, s92
	s_addc_u32 s93, s53, 0
	s_mul_i32 s95, s91, 0x1400
	s_add_i32 s90, s95, 0x11940
	s_add_i32 s95, s95, 0x10000
	s_cmp_lt_u32 s91, 5
	s_cselect_b32 s95, s95, s90
	v_mbcnt_lo_u32_b32 v9, -1, 0
	v_mbcnt_hi_u32_b32 v9, -1, v9
	v_mul_u32_u24_e32 v8, 0x50, v9
	v_add_u32_e32 v8, s95, v8
	v_sub_f32_e32 v7, v99, v10
	v_sub_f32_e32 v6, v98, v10
	v_sub_f32_e32 v5, v93, v10
	v_sub_f32_e32 v4, v92, v10
	ds_write_b128 v8, v[4:7]
	v_sub_f32_e32 v3, v3, v10
	v_sub_f32_e32 v2, v2, v10
	v_sub_f32_e32 v7, v59, v10
	v_sub_f32_e32 v6, v58, v10
	v_sub_f32_e32 v5, v57, v10
	v_sub_f32_e32 v4, v56, v10
	ds_write_b128 v8, v[4:7] offset:16
	v_sub_f32_e32 v1, v1, v10
	v_sub_f32_e32 v0, v0, v10
	v_sub_f32_e32 v7, v31, v10
	v_sub_f32_e32 v6, v30, v10
	v_sub_f32_e32 v5, v29, v10
	v_sub_f32_e32 v4, v28, v10
	ds_write_b128 v8, v[4:7] offset:32
	ds_write_b128 v8, v[0:3] offset:64
	v_sub_f32_e32 v7, v19, v10
	v_sub_f32_e32 v6, v18, v10
	v_sub_f32_e32 v5, v17, v10
	v_sub_f32_e32 v4, v16, v10
	ds_write_b128 v8, v[4:7] offset:48
	s_mov_b64 exec, -1
	v_mbcnt_lo_u32_b32 v9, -1, 0
	v_mbcnt_hi_u32_b32 v9, -1, v9
	v_lshlrev_b32_e32 v9, 4, v9
	v_add_u32_e32 v8, s95, v9
	v_add_u32_e32 v11, 0x1000, v9
	s_waitcnt lgkmcnt(0)
	ds_read_b128 v[12:15], v8
	ds_read_b128 v[16:19], v8 offset:1024
	ds_read_b128 v[20:23], v8 offset:2048
	ds_read_b128 v[24:27], v8 offset:3072
	ds_read_b128 v[28:31], v8 offset:4096
	v_cmp_gt_i32_e32 vcc, s94, v9
	s_mov_b64 exec, vcc
	s_waitcnt lgkmcnt(4)
	global_store_dwordx4 v9, v[12:15], s[92:93]
	s_sub_i32 s94, s94, 0x400
	v_cmp_gt_i32_e32 vcc, s94, v9
	s_mov_b64 exec, vcc
	s_waitcnt lgkmcnt(3)
	global_store_dwordx4 v9, v[16:19], s[92:93] offset:1024
	s_sub_i32 s94, s94, 0x400
	v_cmp_gt_i32_e32 vcc, s94, v9
	s_mov_b64 exec, vcc
	s_waitcnt lgkmcnt(2)
	global_store_dwordx4 v9, v[20:23], s[92:93] offset:2048
	s_sub_i32 s94, s94, 0x400
	v_cmp_gt_i32_e32 vcc, s94, v9
	s_mov_b64 exec, vcc
	s_waitcnt lgkmcnt(1)
	global_store_dwordx4 v9, v[24:27], s[92:93] offset:3072
	s_sub_i32 s94, s94, 0x400
	v_cmp_gt_i32_e32 vcc, s94, v9
	s_mov_b64 exec, vcc
	s_waitcnt lgkmcnt(0)
	global_store_dwordx4 v11, v[28:31], s[92:93]

	.amdhsa_kernel _Z6k_aggfPKjS0_PKtPKfS4_PtS4_S4_PfPj
		.amdhsa_group_segment_fixed_size 138560
		.amdhsa_private_segment_fixed_size 0
		.amdhsa_kernarg_size 336
		.amdhsa_user_sgpr_count 2
		.amdhsa_user_sgpr_dispatch_ptr 0
		.amdhsa_user_sgpr_queue_ptr 0
		.amdhsa_user_sgpr_kernarg_segment_ptr 1
		.amdhsa_user_sgpr_dispatch_id 0
		.amdhsa_user_sgpr_kernarg_preload_length 0
		.amdhsa_user_sgpr_kernarg_preload_offset 0
		.amdhsa_user_sgpr_private_segment_size 0
		.amdhsa_uses_dynamic_stack 0
		.amdhsa_enable_private_segment 0
		.amdhsa_system_sgpr_workgroup_id_x 1
		.amdhsa_system_sgpr_workgroup_id_y 0
		.amdhsa_system_sgpr_workgroup_id_z 0
		.amdhsa_system_sgpr_workgroup_info 0
		.amdhsa_system_vgpr_workitem_id 0
		.amdhsa_next_free_vgpr 128
		.amdhsa_next_free_sgpr 96
		.amdhsa_accum_offset 128
		.amdhsa_reserve_vcc 1
		.amdhsa_float_round_mode_32 0
		.amdhsa_float_round_mode_16_64 0
		.amdhsa_float_denorm_mode_32 3
		.amdhsa_float_denorm_mode_16_64 3
		.amdhsa_dx10_clamp 1
		.amdhsa_ieee_mode 1
		.amdhsa_fp16_overflow 0
		.amdhsa_tg_split 0
		.amdhsa_exception_fp_ieee_invalid_op 0
		.amdhsa_exception_fp_denorm_src 0
		.amdhsa_exception_fp_ieee_div_zero 0
		.amdhsa_exception_fp_ieee_overflow 0
		.amdhsa_exception_fp_ieee_underflow 0
		.amdhsa_exception_fp_ieee_inexact 0
		.amdhsa_exception_int_div_zero 0
	.end_amdhsa_kernel

amdhsa.kernels:
  - .agpr_count:     0
    .args:
      - .actual_access:  read_only
        .address_space:  global
        .offset:         0
        .size:           8
        .value_kind:     global_buffer
      - .actual_access:  read_only
        .address_space:  global
        .offset:         8
        .size:           8
        .value_kind:     global_buffer
      - .actual_access:  write_only
        .address_space:  global
        .offset:         16
        .size:           8
        .value_kind:     global_buffer
      - .actual_access:  write_only
        .address_space:  global
        .offset:         24
        .size:           8
        .value_kind:     global_buffer
      - .actual_access:  write_only
        .address_space:  global
        .offset:         32
        .size:           8
        .value_kind:     global_buffer
      - .actual_access:  write_only
        .address_space:  global
        .offset:         40
        .size:           8
        .value_kind:     global_buffer
      - .actual_access:  write_only
        .address_space:  global
        .offset:         48
        .size:           8
        .value_kind:     global_buffer
    .group_segment_fixed_size: 107840
    .kernarg_segment_align: 8
    .kernarg_segment_size: 56
    .language:       OpenCL C
    .language_version:
      - 2
      - 0
    .max_flat_workgroup_size: 1024
    .name:           _Z6k_partPKiS0_PjPtS1_S1_S1_
    .private_segment_fixed_size: 0
    .sgpr_count:     50
    .sgpr_spill_count: 0
    .symbol:         _Z6k_partPKiS0_PjPtS1_S1_S1_.kd
    .uniform_work_group_size: 1
    .uses_dynamic_stack: false
    .vgpr_count:     123
    .vgpr_spill_count: 0
    .wavefront_size: 64
  - .agpr_count:     0
    .args:
      - .actual_access:  read_only
        .address_space:  global
        .offset:         0
        .size:           8
        .value_kind:     global_buffer
      - .actual_access:  read_only
        .address_space:  global
        .offset:         8
        .size:           8
        .value_kind:     global_buffer
      - .actual_access:  read_only
        .address_space:  global
        .offset:         16
        .size:           8
        .value_kind:     global_buffer
      - .actual_access:  read_only
        .address_space:  global
        .offset:         24
        .size:           8
        .value_kind:     global_buffer
      - .actual_access:  write_only
        .address_space:  global
        .offset:         32
        .size:           8
        .value_kind:     global_buffer
      - .actual_access:  write_only
        .address_space:  global
        .offset:         40
        .size:           8
        .value_kind:     global_buffer
    .group_segment_fixed_size: 103492
    .kernarg_segment_align: 8
    .kernarg_segment_size: 48
    .language:       OpenCL C
    .language_version:
      - 2
      - 0
    .max_flat_workgroup_size: 320
    .name:           _Z6k_gemmPKfS0_PKtPKjPfPt
    .private_segment_fixed_size: 0
    .sgpr_count:     43
    .sgpr_spill_count: 0
    .symbol:         _Z6k_gemmPKfS0_PKtPKjPfPt.kd
    .uniform_work_group_size: 1
    .uses_dynamic_stack: false
    .vgpr_count:     192
    .vgpr_spill_count: 0
    .wavefront_size: 64
  - .agpr_count:     0
    .args:
      - .actual_access:  read_only
        .address_space:  global
        .offset:         0
        .size:           8
        .value_kind:     global_buffer
      - .actual_access:  read_only
        .address_space:  global
        .offset:         8
        .size:           8
        .value_kind:     global_buffer
      - .actual_access:  read_only
        .address_space:  global
        .offset:         16
        .size:           8
        .value_kind:     global_buffer
      - .actual_access:  read_only
        .address_space:  global
        .offset:         24
        .size:           8
        .value_kind:     global_buffer
      - .actual_access:  read_only
        .address_space:  global
        .offset:         32
        .size:           8
        .value_kind:     global_buffer
      - .address_space:  global
        .offset:         40
        .size:           8
        .value_kind:     global_buffer
      - .actual_access:  read_only
        .address_space:  global
        .offset:         48
        .size:           8
        .value_kind:     global_buffer
      - .actual_access:  read_only
        .address_space:  global
        .offset:         56
        .size:           8
        .value_kind:     global_buffer
      - .actual_access:  write_only
        .address_space:  global
        .offset:         64
        .size:           8
        .value_kind:     global_buffer
      - .address_space:  global
        .offset:         72
        .size:           8
        .value_kind:     global_buffer
      - .offset:         80
        .size:           4
        .value_kind:     hidden_block_count_x
      - .offset:         84
        .size:           4
        .value_kind:     hidden_block_count_y
      - .offset:         88
        .size:           4
        .value_kind:     hidden_block_count_z
      - .offset:         92
        .size:           2
        .value_kind:     hidden_group_size_x
      - .offset:         94
        .size:           2
        .value_kind:     hidden_group_size_y
      - .offset:         96
        .size:           2
        .value_kind:     hidden_group_size_z
      - .offset:         98
        .size:           2
        .value_kind:     hidden_remainder_x
      - .offset:         100
        .size:           2
        .value_kind:     hidden_remainder_y
      - .offset:         102
        .size:           2
        .value_kind:     hidden_remainder_z
      - .offset:         120
        .size:           8
        .value_kind:     hidden_global_offset_x
      - .offset:         128
        .size:           8
        .value_kind:     hidden_global_offset_y
      - .offset:         136
        .size:           8
        .value_kind:     hidden_global_offset_z
      - .offset:         144
        .size:           2
        .value_kind:     hidden_grid_dims
    .group_segment_fixed_size: 138560
    .kernarg_segment_align: 8
    .kernarg_segment_size: 336
    .language:       OpenCL C
    .language_version:
      - 2
      - 0
    .max_flat_workgroup_size: 1024
    .name:           _Z6k_aggfPKjS0_PKtPKfS4_PtS4_S4_PfPj
    .private_segment_fixed_size: 0
    .sgpr_count:     81
    .sgpr_spill_count: 0
    .symbol:         _Z6k_aggfPKjS0_PKtPKfS4_PtS4_S4_PfPj.kd
    .uniform_work_group_size: 1
    .uses_dynamic_stack: false
    .vgpr_count:     128
    .vgpr_spill_count: 0
    .wavefront_size: 64
